# NA step: the 64 bias LDS addresses use 8 per-step base registers + immediate row offsets (56 fewer VALU per step and wave)
# baseline (speedup 1.0000x reference)
; #define LAS __attribute__((address_space(3)))
; __device__ __forceinline__ void unit(const bf16_t* __restrict__ proj, const float* __restrict__ rpb, bf16_t* __restrict__ ymix, LAS unsigned char* lds, int u, const int tid_in) {
;     ...
;         const int cs = min(max(cq - 8, 0), 48);
;         const unsigned kb0 = 128u * qi + 16u * ((unsigned)g ^ ((unsigned)qi & 7u)), kb1 = 128u * qi + 16u * ((4u + (unsigned)g) ^ ((unsigned)qi & 7u));
;         const LAS float* bias = (const LAS float*)(lds + LRPB);
;         f32x4 sc[16]; float mx = -3.0e38f;
; #pragma unroll
;         for (int kr = 0; kr < 8; ++kr) {
;             const int krow = rs + kr; const unsigned so = (unsigned)(krow % 9) * 8192u + 128u * (unsigned)cb;
;             const int dr = krow - r + 7;
; #pragma unroll
;             for (int h2 = 0; h2 < 2; ++h2) {
;                 f32x4 a = (f32x4){0.f, 0.f, 0.f, 0.f};
;                 a = __builtin_amdgcn_mfma_f32_16x16x32_bf16(*(const LAS bf16x8*)(lds + LKR + so + 2048u * h2 + kb0), qn[0], a, 0, 0, 0);
;                 a = __builtin_amdgcn_mfma_f32_16x16x32_bf16(*(const LAS bf16x8*)(lds + LKR + so + 2048u * h2 + kb1), qn[1], a, 0, 0, 0);
; #pragma unroll
;                 for (int j = 0; j < 4; ++j) {
;                     const int kcol = cb + 16 * h2 + 4 * g + j;
;                     const int dc = min(max(kcol - cq + 15, 0), 30);
;                     const float v = a[j] + bias[dr * 31 + dc];
;                     const bool in = (kcol >= cs) && (kcol < cs + 16);
;                     a[j] = in ? v : -3.0e38f; mx = fmaxf(mx, a[j]);
;                 }
;                 sc[2 * kr + h2] = a;
;             }
;         }
.LBB0_322:
	s_mul_i32 s5, s57, 29
	s_lshr_b32 s5, s5, 8
	s_mul_i32 s5, s5, 9
	s_sub_i32 s5, s57, s5
	s_and_b32 s5, s5, 0xff
	v_max_i32_e32 v32, 8, v40
	v_bitop3_b32 v33, v36, v61, 7 bitop3:0x78
	v_lshl_add_u32 v35, v34, 7, s24
	s_lshl_b32 s5, s5, 13
	v_add_u32_e32 v32, -8, v32
	v_lshlrev_b32_e32 v33, 4, v33
	v_add_u32_e32 v41, s5, v35
	v_min_u32_e32 v51, 48, v32
	v_and_b32_e32 v32, 7, v61
	v_add_u32_e32 v48, v41, v33
	v_bitop3_b32 v32, v36, v32, 4 bitop3:0x36
	v_lshlrev_b32_e32 v58, 2, v36
	ds_read_b128 v[36:39], v48
	ds_read_b128 v[52:55], v48 offset:2048
	v_add_u32_e32 v46, s43, v58
	v_lshlrev_b32_e32 v32, 4, v32
	v_add_u32_e32 v47, 16, v46
	v_sub_u32_e32 v42, v47, v40
	v_add_u32_e32 v41, v41, v32
	v_max_i32_e32 v49, -15, v42
	ds_read_b128 v[42:45], v41
	ds_read_b128 v[66:69], v41 offset:2048
	s_waitcnt lgkmcnt(3)
	v_mfma_f32_16x16x32_bf16 v[36:39], v[36:39], v[28:31], 0
	v_add_u32_e32 v49, 15, v49
	v_min_u32_e32 v49, 30, v49
	v_or_b32_e32 v71, 1, v46
	v_or_b32_e32 v73, 2, v46
	v_or_b32_e32 v75, 3, v46
	v_add_u32_e32 v78, 17, v46
	v_add_u32_e32 v80, 18, v46
	v_add_u32_e32 v82, 19, v46
	s_waitcnt lgkmcnt(1)
	v_mfma_f32_16x16x32_bf16 v[42:45], v[42:45], v[24:27], v[36:39]
	v_lshlrev_b32_e32 v41, 2, v49
	v_sub_u32_e32 v48, v78, v40
	v_sub_u32_e32 v49, v80, v40
	v_sub_u32_e32 v36, v46, v40
	v_sub_u32_e32 v37, v71, v40
	v_sub_u32_e32 v38, v73, v40
	v_sub_u32_e32 v39, v75, v40
	v_sub_u32_e32 v40, v82, v40
	v_max_i32_e32 v36, -15, v36
	v_max_i32_e32 v37, -15, v37
	v_max_i32_e32 v38, -15, v38
	v_max_i32_e32 v39, -15, v39
	v_max_i32_e32 v48, -15, v48
	v_max_i32_e32 v49, -15, v49
	v_max_i32_e32 v40, -15, v40
	s_sub_i32 s8, s57, s55
	v_add_u32_e32 v36, 15, v36
	v_add_u32_e32 v37, 15, v37
	v_add_u32_e32 v38, 15, v38
	v_add_u32_e32 v39, 15, v39
	v_add_u32_e32 v48, 15, v48
	v_add_u32_e32 v49, 15, v49
	v_add_u32_e32 v40, 15, v40
	s_mulk_i32 s8, 0x7c
	v_min_u32_e32 v36, 30, v36
	v_min_u32_e32 v37, 30, v37
	v_min_u32_e32 v38, 30, v38
	v_min_u32_e32 v39, 30, v39
	v_min_u32_e32 v48, 30, v48
	v_min_u32_e32 v49, 30, v49
	v_min_u32_e32 v40, 30, v40
	v_add_u32_e32 v65, 16, v51
	s_add_i32 s8, s39, s8
	v_lshlrev_b32_e32 v36, 2, v36
	v_lshlrev_b32_e32 v37, 2, v37
	v_lshlrev_b32_e32 v38, 2, v38
	v_lshlrev_b32_e32 v39, 2, v39
	v_lshlrev_b32_e32 v48, 2, v48
	v_lshlrev_b32_e32 v49, 2, v49
	v_lshlrev_b32_e32 v50, 2, v40
	v_add_u32_e32 v126, s8, v36
	v_add_u32_e32 v127, s8, v37
	v_add_u32_e32 v128, s8, v38
	v_add_u32_e32 v129, s8, v39
	v_add_u32_e32 v130, s8, v41
	v_add_u32_e32 v131, s8, v48
	v_add_u32_e32 v132, s8, v49
	v_add_u32_e32 v133, s8, v50
	v_cmp_ge_u32_e32 vcc, v46, v51
	v_cmp_lt_u32_e64 s[8:9], v46, v65
	s_add_i32 s56, s57, 1
	s_and_b64 vcc, vcc, s[8:9]
	v_cmp_ge_u32_e64 s[8:9], v71, v51
	v_cmp_lt_u32_e64 s[10:11], v71, v65
	v_mfma_f32_16x16x32_bf16 v[52:55], v[52:55], v[28:31], 0
	s_mul_i32 s22, s56, 57
	s_and_b64 s[8:9], s[8:9], s[10:11]
	v_cmp_ge_u32_e64 s[10:11], v73, v51
	v_cmp_lt_u32_e64 s[12:13], v73, v65
	s_lshr_b32 s22, s22, 9
	s_and_b64 s[10:11], s[10:11], s[12:13]
	v_cmp_ge_u32_e64 s[12:13], v75, v51
	v_cmp_lt_u32_e64 s[14:15], v75, v65
	s_mul_i32 s22, s22, 9
	ds_read_b32 v70, v126 offset:868
	ds_read_b32 v72, v127 offset:868
	ds_read_b32 v74, v128 offset:868
	ds_read_b32 v76, v129 offset:868
	ds_read_b32 v77, v130 offset:868
	ds_read_b32 v79, v131 offset:868
	ds_read_b32 v81, v132 offset:868
	ds_read_b32 v83, v133 offset:868
	s_and_b64 s[12:13], s[12:13], s[14:15]
	v_cmp_ge_u32_e64 s[14:15], v47, v51
	v_cmp_lt_u32_e64 s[16:17], v46, v51
	s_sub_i32 s22, s56, s22
	s_waitcnt lgkmcnt(8)
	v_mfma_f32_16x16x32_bf16 v[52:55], v[66:69], v[24:27], v[52:55]
	s_and_b64 s[14:15], s[14:15], s[16:17]
	v_cmp_ge_u32_e64 s[16:17], v78, v51
	v_cmp_lt_u32_e64 s[18:19], v78, v65
	s_and_b32 s22, s22, 0xff
	s_and_b64 s[16:17], s[16:17], s[18:19]
	v_cmp_ge_u32_e64 s[18:19], v80, v51
	v_cmp_lt_u32_e64 s[20:21], v80, v65
	s_lshl_b32 s53, s22, 13
	s_and_b64 s[18:19], s[18:19], s[20:21]
	v_cmp_ge_u32_e64 s[20:21], v82, v51
	v_add_u32_e32 v51, s53, v35
	s_waitcnt lgkmcnt(7)
	v_add_f32_e32 v40, v42, v70
	s_waitcnt lgkmcnt(6)
	v_add_f32_e32 v42, v43, v72
	v_add_u32_e32 v72, v51, v33
	s_waitcnt lgkmcnt(5)
	v_add_f32_e32 v43, v44, v74
	s_waitcnt lgkmcnt(4)
	v_add_f32_e32 v44, v45, v76
	s_waitcnt lgkmcnt(3)
	v_add_f32_e32 v45, v52, v77
	s_waitcnt lgkmcnt(2)
	v_add_f32_e32 v46, v53, v79
	s_waitcnt lgkmcnt(1)
	v_add_f32_e32 v47, v54, v81
	s_waitcnt lgkmcnt(0)
	v_add_f32_e32 v71, v55, v83
	ds_read_b128 v[52:55], v72
	v_cndmask_b32_e32 v40, v62, v40, vcc
	v_cndmask_b32_e64 v42, v62, v42, s[8:9]
	v_max3_f32 v70, v40, s40, v42
	v_cndmask_b32_e64 v43, v62, v43, s[10:11]
	v_cndmask_b32_e64 v44, v62, v44, s[12:13]
	v_cmp_lt_u32_e64 s[22:23], v82, v65
	v_max3_f32 v70, v70, v43, v44
	v_cndmask_b32_e64 v45, v62, v45, s[14:15]
	v_cndmask_b32_e64 v46, v62, v46, s[16:17]
	v_add_u32_e32 v65, v51, v32
	s_and_b64 s[20:21], s[20:21], s[22:23]
	v_max3_f32 v70, v70, v45, v46
	v_cndmask_b32_e64 v47, v62, v47, s[18:19]
	ds_read_b128 v[66:69], v65
	ds_read_b128 v[74:77], v65 offset:2048
	v_cndmask_b32_e64 v51, v62, v71, s[20:21]
	v_max3_f32 v82, v70, v47, v51
	ds_read_b128 v[70:73], v72 offset:2048
	s_waitcnt lgkmcnt(3)
	v_mfma_f32_16x16x32_bf16 v[52:55], v[52:55], v[28:31], 0
	s_sub_i32 s22, s56, s55
	s_mulk_i32 s22, 0x7c
	s_add_i32 s22, s39, s22
	s_waitcnt lgkmcnt(2)
	v_mfma_f32_16x16x32_bf16 v[78:81], v[66:69], v[24:27], v[52:55]
	ds_read_b32 v52, v126 offset:992
	ds_read_b32 v53, v127 offset:992
	ds_read_b32 v54, v128 offset:992
	ds_read_b32 v83, v129 offset:992
	ds_read_b32 v65, v130 offset:992
	ds_read_b32 v84, v131 offset:992
	ds_read_b32 v85, v132 offset:992
	ds_read_b32 v86, v133 offset:992
	s_waitcnt lgkmcnt(8)
; #define LAS __attribute__((address_space(3)))
; __device__ __forceinline__ void unit(const bf16_t* __restrict__ proj, const float* __restrict__ rpb, bf16_t* __restrict__ ymix, LAS unsigned char* lds, int u, const int tid_in) {
;     ...
; #pragma unroll
;         for (int kr = 0; kr < 8; ++kr) {
;             const int krow = rs + kr; const unsigned so = (unsigned)(krow % 9) * 8192u + 128u * (unsigned)cb;
;             const int dr = krow - r + 7;
; #pragma unroll
;             for (int h2 = 0; h2 < 2; ++h2) {
;                 f32x4 a = (f32x4){0.f, 0.f, 0.f, 0.f};
;                 a = __builtin_amdgcn_mfma_f32_16x16x32_bf16(*(const LAS bf16x8*)(lds + LKR + so + 2048u * h2 + kb0), qn[0], a, 0, 0, 0);
;                 a = __builtin_amdgcn_mfma_f32_16x16x32_bf16(*(const LAS bf16x8*)(lds + LKR + so + 2048u * h2 + kb1), qn[1], a, 0, 0, 0);
; #pragma unroll
;                 for (int j = 0; j < 4; ++j) {
;                     const int kcol = cb + 16 * h2 + 4 * g + j;
;                     const int dc = min(max(kcol - cq + 15, 0), 30);
;                     const float v = a[j] + bias[dr * 31 + dc];
;                     const bool in = (kcol >= cs) && (kcol < cs + 16);
;                     a[j] = in ? v : -3.0e38f; mx = fmaxf(mx, a[j]);
;                 }
;                 sc[2 * kr + h2] = a;
;             }
;         }
	v_mfma_f32_16x16x32_bf16 v[68:71], v[70:73], v[28:31], 0
	s_mul_i32 s60, s57, 57
	s_add_i32 s22, s60, 0x72
	s_waitcnt lgkmcnt(7)
	v_add_f32_e32 v52, v78, v52
	v_mfma_f32_16x16x32_bf16 v[68:71], v[74:77], v[24:27], v[68:71]
	s_lshr_b32 s22, s22, 9
	v_cndmask_b32_e32 v67, v62, v52, vcc
	s_waitcnt lgkmcnt(6)
	v_add_f32_e32 v52, v79, v53
	s_waitcnt lgkmcnt(5)
	v_add_f32_e32 v53, v80, v54
	s_add_i32 s23, s57, 2
	s_mul_i32 s22, s22, 9
	v_cndmask_b32_e64 v66, v62, v52, s[8:9]
	v_cndmask_b32_e64 v55, v62, v53, s[10:11]
	s_waitcnt lgkmcnt(4)
	v_add_f32_e32 v53, v81, v83
	s_sub_i32 s22, s23, s22
	v_max3_f32 v52, v82, v67, v66
	v_cndmask_b32_e64 v54, v62, v53, s[12:13]
	s_and_b32 s22, s22, 0xff
	v_max3_f32 v72, v52, v55, v54
	s_waitcnt lgkmcnt(3)
	v_add_f32_e32 v52, v68, v65
	s_lshl_b32 s22, s22, 13
	v_cndmask_b32_e64 v53, v62, v52, s[14:15]
	s_waitcnt lgkmcnt(2)
	v_add_f32_e32 v52, v69, v84
	v_add_u32_e32 v69, s22, v35
	v_cndmask_b32_e64 v52, v62, v52, s[16:17]
	s_waitcnt lgkmcnt(1)
	v_add_f32_e32 v68, v70, v85
	v_add_u32_e32 v70, v69, v33
	v_max3_f32 v65, v72, v53, v52
	ds_read_b128 v[72:75], v70
	ds_read_b128 v[80:83], v70 offset:2048
	v_add_u32_e32 v84, v69, v32
	ds_read_b128 v[76:79], v84
	s_waitcnt lgkmcnt(3)
	v_add_f32_e32 v71, v71, v86
	v_cndmask_b32_e64 v69, v62, v71, s[20:21]
	s_waitcnt lgkmcnt(2)
	v_mfma_f32_16x16x32_bf16 v[70:73], v[72:75], v[28:31], 0
	ds_read_b128 v[84:87], v84 offset:2048
	s_sub_i32 s23, s23, s55
	s_mulk_i32 s23, 0x7c
	s_waitcnt lgkmcnt(1)
	v_mfma_f32_16x16x32_bf16 v[76:79], v[76:79], v[24:27], v[70:73]
	s_add_i32 s23, s39, s23
	ds_read_b32 v70, v126 offset:1116
	ds_read_b32 v71, v127 offset:1116
	ds_read_b32 v72, v128 offset:1116
	ds_read_b32 v90, v129 offset:1116
	ds_read_b32 v91, v130 offset:1116
	ds_read_b32 v92, v131 offset:1116
	ds_read_b32 v88, v132 offset:1116
	ds_read_b32 v89, v133 offset:1116
	v_mfma_f32_16x16x32_bf16 v[80:83], v[80:83], v[28:31], 0
	s_waitcnt lgkmcnt(7)
	v_add_f32_e32 v70, v76, v70
	v_cndmask_b32_e32 v75, v62, v70, vcc
	s_waitcnt lgkmcnt(6)
	v_add_f32_e32 v70, v77, v71
	v_cndmask_b32_e64 v74, v62, v70, s[8:9]
	s_waitcnt lgkmcnt(5)
	v_add_f32_e32 v70, v78, v72
	s_add_i32 s23, s60, 0xab
	v_cndmask_b32_e64 v73, v62, v70, s[10:11]
	s_waitcnt lgkmcnt(4)
	v_add_f32_e32 v70, v79, v90
	v_mfma_f32_16x16x32_bf16 v[76:79], v[84:87], v[24:27], v[80:83]
	s_lshr_b32 s23, s23, 9
	s_add_i32 s56, s57, 3
	s_mul_i32 s23, s23, 9
	s_sub_i32 s23, s56, s23
	s_and_b32 s23, s23, 0xff
	v_cndmask_b32_e64 v72, v62, v70, s[12:13]
	s_waitcnt lgkmcnt(3)
	s_nop 0
	v_add_f32_e32 v70, v76, v91
	s_lshl_b32 s23, s23, 13
	v_cndmask_b32_e64 v71, v62, v70, s[14:15]
	s_waitcnt lgkmcnt(2)
	v_add_f32_e32 v70, v77, v92
	v_add_u32_e32 v77, s23, v35
	s_waitcnt lgkmcnt(1)
	v_add_f32_e32 v76, v78, v88
	v_add_u32_e32 v78, v77, v33
	ds_read_b128 v[80:83], v78
	v_add_u32_e32 v92, v77, v32
	ds_read_b128 v[84:87], v92
	s_waitcnt lgkmcnt(2)
	v_add_f32_e32 v79, v79, v89
	ds_read_b128 v[88:91], v78 offset:2048
	v_cndmask_b32_e64 v77, v62, v79, s[20:21]
	s_waitcnt lgkmcnt(2)
	v_mfma_f32_16x16x32_bf16 v[78:81], v[80:83], v[28:31], 0
	ds_read_b128 v[92:95], v92 offset:2048
	s_sub_i32 s56, s56, s55
	s_mulk_i32 s56, 0x7c
	s_waitcnt lgkmcnt(2)
	v_mfma_f32_16x16x32_bf16 v[84:87], v[84:87], v[24:27], v[78:81]
	s_add_i32 s56, s39, s56
	ds_read_b32 v78, v126 offset:1240
	ds_read_b32 v79, v127 offset:1240
	ds_read_b32 v80, v128 offset:1240
	ds_read_b32 v98, v129 offset:1240
	ds_read_b32 v99, v130 offset:1240
	ds_read_b32 v100, v131 offset:1240
	ds_read_b32 v96, v132 offset:1240
	ds_read_b32 v97, v133 offset:1240
	s_waitcnt lgkmcnt(9)
	v_mfma_f32_16x16x32_bf16 v[88:91], v[88:91], v[28:31], 0
	s_waitcnt lgkmcnt(7)
	v_add_f32_e32 v78, v84, v78
	v_cndmask_b32_e32 v83, v62, v78, vcc
	s_waitcnt lgkmcnt(6)
	v_add_f32_e32 v78, v85, v79
	v_cndmask_b32_e64 v82, v62, v78, s[8:9]
	s_waitcnt lgkmcnt(5)
	v_add_f32_e32 v78, v86, v80
	s_add_i32 s56, s60, 0xe4
	v_cndmask_b32_e64 v81, v62, v78, s[10:11]
	s_waitcnt lgkmcnt(4)
	v_add_f32_e32 v78, v87, v98
	v_mfma_f32_16x16x32_bf16 v[84:87], v[92:95], v[24:27], v[88:91]
	s_lshr_b32 s56, s56, 9
	s_add_i32 s58, s57, 4
	s_mul_i32 s56, s56, 9
	s_sub_i32 s56, s58, s56
	s_and_b32 s56, s56, 0xff
	v_cndmask_b32_e64 v80, v62, v78, s[12:13]
	s_waitcnt lgkmcnt(3)
	s_nop 0
	v_add_f32_e32 v78, v84, v99
	s_lshl_b32 s56, s56, 13
	v_cndmask_b32_e64 v79, v62, v78, s[14:15]
	s_waitcnt lgkmcnt(2)
	v_add_f32_e32 v78, v85, v100
	v_add_u32_e32 v85, s56, v35
	s_waitcnt lgkmcnt(1)
	v_add_f32_e32 v84, v86, v96
	v_add_u32_e32 v86, v85, v33
	ds_read_b128 v[88:91], v86
	v_add_u32_e32 v100, v85, v32
	ds_read_b128 v[92:95], v100
	s_waitcnt lgkmcnt(2)
	v_add_f32_e32 v87, v87, v97
	v_cndmask_b32_e64 v85, v62, v87, s[20:21]
	ds_read_b128 v[96:99], v86 offset:2048
	s_waitcnt lgkmcnt(2)
	v_mfma_f32_16x16x32_bf16 v[86:89], v[88:91], v[28:31], 0
	s_sub_i32 s58, s58, s55
	s_mulk_i32 s58, 0x7c
	ds_read_b128 v[100:103], v100 offset:2048
	s_waitcnt lgkmcnt(2)
	v_mfma_f32_16x16x32_bf16 v[86:89], v[92:95], v[24:27], v[86:89]
	s_add_i32 s58, s39, s58
	ds_read_b32 v90, v126 offset:1364
	ds_read_b32 v91, v127 offset:1364
	ds_read_b32 v92, v128 offset:1364
	ds_read_b32 v106, v129 offset:1364
	ds_read_b32 v94, v130 offset:1364
	ds_read_b32 v95, v131 offset:1364
	ds_read_b32 v104, v132 offset:1364
	ds_read_b32 v105, v133 offset:1364
	s_waitcnt lgkmcnt(7)
	v_add_f32_e32 v86, v86, v90
	v_cndmask_b32_e32 v107, v62, v86, vcc
	s_waitcnt lgkmcnt(6)
	v_add_f32_e32 v86, v87, v91
	v_cndmask_b32_e64 v108, v62, v86, s[8:9]
	s_waitcnt lgkmcnt(5)
	v_add_f32_e32 v86, v88, v92
	v_mfma_f32_16x16x32_bf16 v[90:93], v[96:99], v[28:31], 0
	v_cndmask_b32_e64 v109, v62, v86, s[10:11]
	s_waitcnt lgkmcnt(4)
; #define LAS __attribute__((address_space(3)))
; __device__ __forceinline__ void unit(const bf16_t* __restrict__ proj, const float* __restrict__ rpb, bf16_t* __restrict__ ymix, LAS unsigned char* lds, int u, const int tid_in) {
;     ...
; #pragma unroll
;         for (int kr = 0; kr < 8; ++kr) {
;             const int krow = rs + kr; const unsigned so = (unsigned)(krow % 9) * 8192u + 128u * (unsigned)cb;
;             const int dr = krow - r + 7;
; #pragma unroll
;             for (int h2 = 0; h2 < 2; ++h2) {
;                 f32x4 a = (f32x4){0.f, 0.f, 0.f, 0.f};
;                 a = __builtin_amdgcn_mfma_f32_16x16x32_bf16(*(const LAS bf16x8*)(lds + LKR + so + 2048u * h2 + kb0), qn[0], a, 0, 0, 0);
;                 a = __builtin_amdgcn_mfma_f32_16x16x32_bf16(*(const LAS bf16x8*)(lds + LKR + so + 2048u * h2 + kb1), qn[1], a, 0, 0, 0);
; #pragma unroll
;                 for (int j = 0; j < 4; ++j) {
;                     const int kcol = cb + 16 * h2 + 4 * g + j;
;                     const int dc = min(max(kcol - cq + 15, 0), 30);
;                     const float v = a[j] + bias[dr * 31 + dc];
;                     const bool in = (kcol >= cs) && (kcol < cs + 16);
;                     a[j] = in ? v : -3.0e38f; mx = fmaxf(mx, a[j]);
;                 }
;                 sc[2 * kr + h2] = a;
;             }
;         }
	v_add_f32_e32 v86, v89, v106
	s_add_i32 s58, s60, 0x11d
	v_cndmask_b32_e64 v106, v62, v86, s[12:13]
	v_mfma_f32_16x16x32_bf16 v[86:89], v[100:103], v[24:27], v[90:93]
	s_lshr_b32 s58, s58, 9
	s_add_i32 s59, s57, 5
	s_mul_i32 s58, s58, 9
	s_sub_i32 s58, s59, s58
	s_and_b32 s58, s58, 0xff
	s_waitcnt lgkmcnt(3)
	s_nop 1
	v_add_f32_e32 v86, v86, v94
	s_lshl_b32 s58, s58, 13
	v_cndmask_b32_e64 v102, v62, v86, s[14:15]
	s_waitcnt lgkmcnt(2)
	v_add_f32_e32 v86, v87, v95
	v_add_u32_e32 v87, s58, v35
	v_add_u32_e32 v94, v87, v33
	ds_read_b128 v[90:93], v94
	v_cndmask_b32_e64 v103, v62, v86, s[16:17]
	s_waitcnt lgkmcnt(2)
	v_add_f32_e32 v86, v88, v104
	v_add_u32_e32 v98, v87, v32
	v_cndmask_b32_e64 v104, v62, v86, s[18:19]
	s_waitcnt lgkmcnt(1)
	v_add_f32_e32 v95, v89, v105
	ds_read_b128 v[86:89], v98
	s_waitcnt lgkmcnt(1)
	v_mfma_f32_16x16x32_bf16 v[90:93], v[90:93], v[28:31], 0
	v_cndmask_b32_e64 v105, v62, v95, s[20:21]
	ds_read_b128 v[94:97], v94 offset:2048
	ds_read_b128 v[98:101], v98 offset:2048
	s_sub_i32 s59, s59, s55
	s_waitcnt lgkmcnt(2)
	v_mfma_f32_16x16x32_bf16 v[86:89], v[86:89], v[24:27], v[90:93]
	s_mulk_i32 s59, 0x7c
	s_add_i32 s59, s39, s59
	s_nop 0
	ds_read_b32 v90, v126 offset:1488
	ds_read_b32 v91, v127 offset:1488
	ds_read_b32 v92, v128 offset:1488
	ds_read_b32 v114, v129 offset:1488
	ds_read_b32 v110, v130 offset:1488
	ds_read_b32 v111, v131 offset:1488
	ds_read_b32 v112, v132 offset:1488
	ds_read_b32 v113, v133 offset:1488
	s_waitcnt lgkmcnt(7)
	v_add_f32_e32 v86, v86, v90
	v_cndmask_b32_e32 v115, v62, v86, vcc
	s_waitcnt lgkmcnt(6)
	v_add_f32_e32 v86, v87, v91
	v_cndmask_b32_e64 v116, v62, v86, s[8:9]
	s_waitcnt lgkmcnt(5)
	v_add_f32_e32 v86, v88, v92
	v_mfma_f32_16x16x32_bf16 v[90:93], v[94:97], v[28:31], 0
	v_cndmask_b32_e64 v117, v62, v86, s[10:11]
	s_waitcnt lgkmcnt(4)
	v_add_f32_e32 v86, v89, v114
	s_add_i32 s59, s60, 0x156
	v_cndmask_b32_e64 v114, v62, v86, s[12:13]
	v_mfma_f32_16x16x32_bf16 v[86:89], v[98:101], v[24:27], v[90:93]
	s_lshr_b32 s59, s59, 9
	s_add_i32 s61, s57, 6
	s_mul_i32 s59, s59, 9
	s_sub_i32 s59, s61, s59
	s_and_b32 s59, s59, 0xff
	s_waitcnt lgkmcnt(3)
	s_nop 1
	v_add_f32_e32 v86, v86, v110
	s_lshl_b32 s59, s59, 13
	v_cndmask_b32_e64 v110, v62, v86, s[14:15]
	s_waitcnt lgkmcnt(2)
	v_add_f32_e32 v86, v87, v111
	v_add_u32_e32 v87, s59, v35
	v_add_u32_e32 v94, v87, v33
	ds_read_b128 v[90:93], v94
	v_cndmask_b32_e64 v111, v62, v86, s[16:17]
	s_waitcnt lgkmcnt(2)
	v_add_f32_e32 v86, v88, v112
	v_add_u32_e32 v98, v87, v32
	v_cndmask_b32_e64 v112, v62, v86, s[18:19]
	s_waitcnt lgkmcnt(1)
	v_add_f32_e32 v95, v89, v113
	ds_read_b128 v[86:89], v98
	s_waitcnt lgkmcnt(1)
	v_mfma_f32_16x16x32_bf16 v[90:93], v[90:93], v[28:31], 0
	v_cndmask_b32_e64 v113, v62, v95, s[20:21]
	ds_read_b128 v[94:97], v94 offset:2048
	ds_read_b128 v[98:101], v98 offset:2048
	s_sub_i32 s61, s61, s55
	s_waitcnt lgkmcnt(2)
	v_mfma_f32_16x16x32_bf16 v[86:89], v[86:89], v[24:27], v[90:93]
	s_mulk_i32 s61, 0x7c
	s_add_i32 s61, s39, s61
	s_nop 0
	ds_read_b32 v90, v126 offset:1612
	ds_read_b32 v91, v127 offset:1612
	ds_read_b32 v92, v128 offset:1612
	ds_read_b32 v122, v129 offset:1612
	ds_read_b32 v118, v130 offset:1612
	ds_read_b32 v119, v131 offset:1612
	ds_read_b32 v120, v132 offset:1612
	ds_read_b32 v121, v133 offset:1612
	s_waitcnt lgkmcnt(7)
	v_add_f32_e32 v86, v86, v90
	v_cndmask_b32_e32 v123, v62, v86, vcc
	s_waitcnt lgkmcnt(6)
	v_add_f32_e32 v86, v87, v91
	s_addk_i32 s60, 0x18f
	v_cndmask_b32_e64 v124, v62, v86, s[8:9]
	s_waitcnt lgkmcnt(5)
	v_add_f32_e32 v86, v88, v92
	v_mfma_f32_16x16x32_bf16 v[90:93], v[94:97], v[28:31], 0
	s_add_i32 s61, s57, 7
	s_lshr_b32 s57, s60, 9
	s_mul_i32 s57, s57, 9
	s_sub_i32 s57, s61, s57
	v_cndmask_b32_e64 v125, v62, v86, s[10:11]
	s_waitcnt lgkmcnt(4)
	v_add_f32_e32 v86, v89, v122
	s_and_b32 s57, s57, 0xff
	v_cndmask_b32_e64 v122, v62, v86, s[12:13]
	v_mfma_f32_16x16x32_bf16 v[86:89], v[98:101], v[24:27], v[90:93]
	s_lshl_b32 s57, s57, 13
	v_cndmask_b32_e64 v68, v62, v68, s[18:19]
	v_add_u32_e32 v35, s57, v35
	v_max3_f32 v65, v65, v68, v69
	v_add_u32_e32 v33, v35, v33
	v_max3_f32 v65, v65, v75, v74
	ds_read_b128 v[90:93], v33
	v_max3_f32 v65, v65, v73, v72
	v_cndmask_b32_e64 v70, v62, v70, s[16:17]
	s_waitcnt lgkmcnt(4)
	v_add_f32_e32 v86, v86, v118
	s_waitcnt lgkmcnt(1)
	v_add_f32_e32 v94, v89, v121
	v_max3_f32 v65, v65, v71, v70
	v_cndmask_b32_e64 v76, v62, v76, s[18:19]
	v_cndmask_b32_e64 v118, v62, v86, s[14:15]
	v_add_f32_e32 v86, v87, v119
	v_cndmask_b32_e64 v121, v62, v94, s[20:21]
	ds_read_b128 v[94:97], v33 offset:2048
	v_max3_f32 v65, v65, v76, v77
	v_cndmask_b32_e64 v119, v62, v86, s[16:17]
	v_add_f32_e32 v86, v88, v120
	v_add_u32_e32 v32, v35, v32
	v_max3_f32 v65, v65, v83, v82
	v_cndmask_b32_e64 v120, v62, v86, s[18:19]
	ds_read_b128 v[86:89], v32
	ds_read_b128 v[98:101], v32 offset:2048
	v_max3_f32 v65, v65, v81, v80
	v_cndmask_b32_e64 v78, v62, v78, s[16:17]
	v_max3_f32 v65, v65, v79, v78
	v_cndmask_b32_e64 v84, v62, v84, s[18:19]
	v_max3_f32 v65, v65, v84, v85
	v_max3_f32 v65, v65, v107, v108
	v_max3_f32 v65, v65, v109, v106
	s_waitcnt lgkmcnt(3)
	v_mfma_f32_16x16x32_bf16 v[90:93], v[90:93], v[28:31], 0
	v_max3_f32 v65, v65, v102, v103
	v_max3_f32 v65, v65, v104, v105
	v_max3_f32 v65, v65, v115, v116
	s_waitcnt lgkmcnt(2)
	v_mfma_f32_16x16x32_bf16 v[28:31], v[94:97], v[28:31], 0
	s_sub_i32 s55, s61, s55
	v_max3_f32 v65, v65, v117, v114
	s_mulk_i32 s55, 0x7c
	s_waitcnt lgkmcnt(1)
	v_mfma_f32_16x16x32_bf16 v[86:89], v[86:89], v[24:27], v[90:93]
	v_max3_f32 v65, v65, v110, v111
	s_add_i32 s55, s39, s55
	v_max3_f32 v65, v65, v112, v113
	s_waitcnt lgkmcnt(0)
; #define LAS __attribute__((address_space(3)))
; __device__ __forceinline__ bf16x8 pack8(const float (&f)[8]) { u32x4 u; u.x = cvtpk(f[0], f[1]); u.y = cvtpk(f[2], f[3]); u.z = cvtpk(f[4], f[5]); u.w = cvtpk(f[6], f[7]); return __builtin_bit_cast(bf16x8, u); }
; __device__ __forceinline__ void unit(const bf16_t* __restrict__ proj, const float* __restrict__ rpb, bf16_t* __restrict__ ymix, LAS unsigned char* lds, int u, const int tid_in) {
;     ...
;         for (int kr = 0; kr < 8; ++kr) {
;             const int krow = rs + kr; const unsigned so = (unsigned)(krow % 9) * 8192u + 128u * (unsigned)cb;
;             const int dr = krow - r + 7;
; #pragma unroll
;             for (int h2 = 0; h2 < 2; ++h2) {
;                 f32x4 a = (f32x4){0.f, 0.f, 0.f, 0.f};
;                 a = __builtin_amdgcn_mfma_f32_16x16x32_bf16(*(const LAS bf16x8*)(lds + LKR + so + 2048u * h2 + kb0), qn[0], a, 0, 0, 0);
;                 a = __builtin_amdgcn_mfma_f32_16x16x32_bf16(*(const LAS bf16x8*)(lds + LKR + so + 2048u * h2 + kb1), qn[1], a, 0, 0, 0);
; #pragma unroll
;                 for (int j = 0; j < 4; ++j) {
;                     const int kcol = cb + 16 * h2 + 4 * g + j;
;                     const int dc = min(max(kcol - cq + 15, 0), 30);
;                     const float v = a[j] + bias[dr * 31 + dc];
;                     const bool in = (kcol >= cs) && (kcol < cs + 16);
;                     a[j] = in ? v : -3.0e38f; mx = fmaxf(mx, a[j]);
;                 }
;                 sc[2 * kr + h2] = a;
;             }
;         }
;         mx = fmaxf(mx, __shfl_xor(mx, 16)); mx = fmaxf(mx, __shfl_xor(mx, 32));
;         float sum = 0.f; bf16x8 pt[8];
; #pragma unroll
;         for (int kk = 0; kk < 8; ++kk) {
;             float pv[8];
; #pragma unroll
;             for (int h2 = 0; h2 < 2; ++h2)
; #pragma unroll
;                 for (int j = 0; j < 4; ++j) { const float e = __builtin_amdgcn_exp2f((sc[2 * kk + h2][j] - mx) * 1.4426950408889634f); pv[4 * h2 + j] = e; sum += e; }
;             pt[kk] = ret::pack8(pv);
;         }
;         sum += __shfl_xor(sum, 16); sum += __shfl_xor(sum, 32);
	v_mfma_f32_16x16x32_bf16 v[24:27], v[98:101], v[24:27], v[28:31]
	v_max3_f32 v65, v65, v123, v124
	ds_read_b32 v32, v126 offset:1736
	ds_read_b32 v33, v127 offset:1736
	ds_read_b32 v36, v128 offset:1736
	ds_read_b32 v37, v129 offset:1736
	ds_read_b32 v38, v130 offset:1736
	ds_read_b32 v39, v131 offset:1736
	ds_read_b32 v41, v132 offset:1736
	ds_read_b32 v48, v133 offset:1736
	v_max3_f32 v65, v65, v125, v122
	s_waitcnt lgkmcnt(7)
	v_add_f32_e32 v32, v86, v32
	v_max3_f32 v65, v65, v118, v119
	v_cndmask_b32_e32 v49, v62, v32, vcc
	s_waitcnt lgkmcnt(6)
	v_add_f32_e32 v32, v87, v33
	s_waitcnt lgkmcnt(5)
	v_add_f32_e32 v33, v88, v36
	v_max3_f32 v35, v65, v120, v121
	v_cndmask_b32_e64 v50, v62, v32, s[8:9]
	v_cndmask_b32_e64 v86, v62, v33, s[10:11]
	s_waitcnt lgkmcnt(4)
	v_add_f32_e32 v33, v89, v37
	s_waitcnt lgkmcnt(3)
	v_add_f32_e32 v24, v24, v38
	v_max3_f32 v32, v35, v49, v50
	v_cndmask_b32_e64 v87, v62, v33, s[12:13]
	v_cndmask_b32_e64 v88, v62, v24, s[14:15]
	s_waitcnt lgkmcnt(2)
	v_add_f32_e32 v24, v25, v39
	s_waitcnt lgkmcnt(1)
	v_add_f32_e32 v25, v26, v41
	v_max3_f32 v32, v32, v86, v87
	v_cndmask_b32_e64 v89, v62, v24, s[16:17]
	v_cndmask_b32_e64 v90, v62, v25, s[18:19]
	s_waitcnt lgkmcnt(0)
	v_add_f32_e32 v25, v27, v48
	v_max3_f32 v24, v32, v88, v89
	v_cndmask_b32_e64 v48, v62, v25, s[20:21]
	v_max3_f32 v24, v24, v90, v48
	ds_bpermute_b32 v25, v195, v24
	v_lshrrev_b32_e32 v65, 2, v34
	v_lshrrev_b32_e32 v91, 4, v61
	v_lshlrev_b32_e32 v92, 3, v61
	s_add_i32 s5, s50, s5
	s_waitcnt lgkmcnt(0)
	v_max_f32_e32 v25, v25, v25
	v_max_f32_e32 v24, v24, v25
	ds_bpermute_b32 v25, v196, v24
	s_add_i32 s9, s50, s53
	s_add_i32 s12, s50, s56
	s_add_i32 s13, s50, s58
	s_add_i32 s14, s50, s59
	s_waitcnt lgkmcnt(0)
	v_max_f32_e32 v25, v25, v25
	v_max_f32_e32 v93, v24, v25
	v_sub_f32_e32 v24, v40, v93
	v_mul_f32_e32 v24, 0x3fb8aa3b, v24
	v_sub_f32_e32 v25, v42, v93
	v_exp_f32_e32 v24, v24
	v_mul_f32_e32 v25, 0x3fb8aa3b, v25
	v_sub_f32_e32 v26, v43, v93
	v_exp_f32_e32 v25, v25
	v_mul_f32_e32 v26, 0x3fb8aa3b, v26
	v_sub_f32_e32 v27, v44, v93
	v_exp_f32_e32 v26, v26
	v_mul_f32_e32 v27, 0x3fb8aa3b, v27
	v_sub_f32_e32 v29, v45, v93
	v_sub_f32_e32 v30, v46, v93
	v_exp_f32_e32 v27, v27
	v_mul_f32_e32 v29, 0x3fb8aa3b, v29
	v_mul_f32_e32 v30, 0x3fb8aa3b, v30
	v_add_f32_e32 v28, 0, v24
	v_exp_f32_e32 v29, v29
	v_exp_f32_e32 v30, v30
	v_sub_f32_e32 v31, v47, v93
	v_sub_f32_e32 v32, v51, v93
	v_add_f32_e32 v28, v25, v28
	v_mul_f32_e32 v31, 0x3fb8aa3b, v31
	v_mul_f32_e32 v32, 0x3fb8aa3b, v32
	v_add_f32_e32 v28, v26, v28
	v_exp_f32_e32 v31, v31
	v_exp_f32_e32 v32, v32
	v_add_f32_e32 v28, v27, v28
	v_add_f32_e32 v28, v29, v28
	v_cvt_pk_bf16_f32 v24, v24, v25
	v_cvt_pk_bf16_f32 v25, v26, v27
	v_cvt_pk_bf16_f32 v26, v29, v30
	v_sub_f32_e32 v29, v67, v93
	v_add_f32_e32 v28, v30, v28
	v_mul_f32_e32 v29, 0x3fb8aa3b, v29
	v_sub_f32_e32 v30, v66, v93
	v_add_f32_e32 v28, v31, v28
	v_cvt_pk_bf16_f32 v27, v31, v32
	v_exp_f32_e32 v29, v29
	v_mul_f32_e32 v30, 0x3fb8aa3b, v30
	v_sub_f32_e32 v31, v55, v93
	v_add_f32_e32 v28, v32, v28
	v_exp_f32_e32 v30, v30
	v_mul_f32_e32 v31, 0x3fb8aa3b, v31
	v_sub_f32_e32 v32, v54, v93
	v_exp_f32_e32 v31, v31
	v_mul_f32_e32 v32, 0x3fb8aa3b, v32
	v_sub_f32_e32 v33, v53, v93
	v_exp_f32_e32 v32, v32
	v_mul_f32_e32 v33, 0x3fb8aa3b, v33
	v_sub_f32_e32 v34, v52, v93
	v_add_f32_e32 v28, v29, v28
	v_exp_f32_e32 v33, v33
	v_mul_f32_e32 v34, 0x3fb8aa3b, v34
	v_sub_f32_e32 v35, v68, v93
	v_add_f32_e32 v28, v30, v28
	v_exp_f32_e32 v34, v34
	v_mul_f32_e32 v35, 0x3fb8aa3b, v35
	v_sub_f32_e32 v36, v69, v93
	v_add_f32_e32 v28, v31, v28
	v_exp_f32_e32 v35, v35
	v_mul_f32_e32 v36, 0x3fb8aa3b, v36
	v_add_f32_e32 v28, v32, v28
	v_exp_f32_e32 v36, v36
	v_add_f32_e32 v28, v33, v28
	v_add_f32_e32 v28, v34, v28
	v_add_f32_e32 v28, v35, v28
	v_add_f32_e32 v37, v36, v28
	v_cvt_pk_bf16_f32 v28, v29, v30
	v_cvt_pk_bf16_f32 v29, v31, v32
	v_sub_f32_e32 v32, v75, v93
	v_mul_f32_e32 v32, 0x3fb8aa3b, v32
	v_exp_f32_e32 v32, v32
	v_cvt_pk_bf16_f32 v30, v33, v34
	v_sub_f32_e32 v33, v74, v93
	v_mul_f32_e32 v33, 0x3fb8aa3b, v33
	v_sub_f32_e32 v34, v73, v93
	v_cvt_pk_bf16_f32 v31, v35, v36
	v_exp_f32_e32 v33, v33
	v_mul_f32_e32 v34, 0x3fb8aa3b, v34
	v_sub_f32_e32 v35, v72, v93
	v_exp_f32_e32 v34, v34
	v_mul_f32_e32 v35, 0x3fb8aa3b, v35
	v_add_f32_e32 v36, v32, v37
	v_sub_f32_e32 v37, v71, v93
	v_sub_f32_e32 v38, v70, v93
	v_exp_f32_e32 v35, v35
	v_mul_f32_e32 v37, 0x3fb8aa3b, v37
	v_mul_f32_e32 v38, 0x3fb8aa3b, v38
	v_exp_f32_e32 v37, v37
	v_exp_f32_e32 v38, v38
	v_sub_f32_e32 v39, v76, v93
	v_sub_f32_e32 v40, v77, v93
	v_add_f32_e32 v36, v33, v36
	v_mul_f32_e32 v39, 0x3fb8aa3b, v39
	v_mul_f32_e32 v40, 0x3fb8aa3b, v40
	v_add_f32_e32 v36, v34, v36
	v_exp_f32_e32 v39, v39
	v_exp_f32_e32 v40, v40
	v_add_f32_e32 v36, v35, v36
	v_add_f32_e32 v36, v37, v36
	v_cvt_pk_bf16_f32 v32, v32, v33
	v_cvt_pk_bf16_f32 v33, v34, v35
	v_cvt_pk_bf16_f32 v34, v37, v38
	v_sub_f32_e32 v37, v83, v93
	v_add_f32_e32 v36, v38, v36
	v_mul_f32_e32 v37, 0x3fb8aa3b, v37
	v_sub_f32_e32 v38, v82, v93
	v_add_f32_e32 v36, v39, v36
	v_cvt_pk_bf16_f32 v35, v39, v40
	v_exp_f32_e32 v37, v37
	v_mul_f32_e32 v38, 0x3fb8aa3b, v38
	v_sub_f32_e32 v39, v81, v93
	v_add_f32_e32 v36, v40, v36
	v_exp_f32_e32 v38, v38
	v_mul_f32_e32 v39, 0x3fb8aa3b, v39
	v_sub_f32_e32 v40, v80, v93
	v_exp_f32_e32 v39, v39
	v_mul_f32_e32 v40, 0x3fb8aa3b, v40
	v_sub_f32_e32 v41, v79, v93
	v_exp_f32_e32 v40, v40
	v_mul_f32_e32 v41, 0x3fb8aa3b, v41
	v_sub_f32_e32 v42, v78, v93
	v_add_f32_e32 v36, v37, v36
	v_exp_f32_e32 v41, v41
	v_mul_f32_e32 v42, 0x3fb8aa3b, v42
	v_sub_f32_e32 v43, v84, v93
	v_add_f32_e32 v36, v38, v36
	v_exp_f32_e32 v42, v42
; #define LAS __attribute__((address_space(3)))
; __device__ __forceinline__ bf16x8 pack8(const float (&f)[8]) { u32x4 u; u.x = cvtpk(f[0], f[1]); u.y = cvtpk(f[2], f[3]); u.z = cvtpk(f[4], f[5]); u.w = cvtpk(f[6], f[7]); return __builtin_bit_cast(bf16x8, u); }
; __device__ __forceinline__ void unit(const bf16_t* __restrict__ proj, const float* __restrict__ rpb, bf16_t* __restrict__ ymix, LAS unsigned char* lds, int u, const int tid_in) {
;     ...
;         float sum = 0.f; bf16x8 pt[8];
; #pragma unroll
;         for (int kk = 0; kk < 8; ++kk) {
;             float pv[8];
; #pragma unroll
;             for (int h2 = 0; h2 < 2; ++h2)
; #pragma unroll
;                 for (int j = 0; j < 4; ++j) { const float e = __builtin_amdgcn_exp2f((sc[2 * kk + h2][j] - mx) * 1.4426950408889634f); pv[4 * h2 + j] = e; sum += e; }
;             pt[kk] = ret::pack8(pv);
;         }
;         sum += __shfl_xor(sum, 16); sum += __shfl_xor(sum, 32);
;         const float inv = 1.f / sum;
;         const unsigned sl = (((unsigned)g & 1u) << 2) | qp;
;         unsigned char* op = (unsigned char*)ymix + (size_t)tq * D + head * 64 + 4 * g;
; #pragma unroll
;         for (int db = 0; db < 4; ++db) {
;             const unsigned vb = 128u * (4u * (unsigned)g + qp) + 16u * ((2u * db + (p >> 1)) ^ sl) + 8u * (p & 1u);
;             f32x4 y = (f32x4){0.f, 0.f, 0.f, 0.f};
; #pragma unroll
;             for (int kk = 0; kk < 8; ++kk) {
;                 const unsigned so = (unsigned)((rs + kk) % 9) * 8192u + 128u * (unsigned)cb;
;                 const ret::s16x4 lo = __builtin_amdgcn_ds_read_tr16_b64_v4i16((LAS ret::s16x4*)(lds + LVR + so + vb));
;                 const ret::s16x4 hi = __builtin_amdgcn_ds_read_tr16_b64_v4i16((LAS ret::s16x4*)(lds + LVR + so + 2048u + vb));
;                 y = __builtin_amdgcn_mfma_f32_16x16x32_bf16(__builtin_shufflevector(lo, hi, 0, 1, 2, 3, 4, 5, 6, 7), pt[kk], y, 0, 0, 0);
	v_mul_f32_e32 v43, 0x3fb8aa3b, v43
	v_sub_f32_e32 v44, v85, v93
	v_add_f32_e32 v36, v39, v36
	v_exp_f32_e32 v43, v43
	v_mul_f32_e32 v44, 0x3fb8aa3b, v44
	v_add_f32_e32 v36, v40, v36
	v_exp_f32_e32 v44, v44
	v_add_f32_e32 v36, v41, v36
	v_add_f32_e32 v36, v42, v36
	v_add_f32_e32 v36, v43, v36
	v_add_f32_e32 v45, v44, v36
	v_cvt_pk_bf16_f32 v36, v37, v38
	v_cvt_pk_bf16_f32 v37, v39, v40
	v_sub_f32_e32 v40, v107, v93
	v_mul_f32_e32 v40, 0x3fb8aa3b, v40
	v_exp_f32_e32 v40, v40
	v_cvt_pk_bf16_f32 v38, v41, v42
	v_sub_f32_e32 v41, v108, v93
	v_mul_f32_e32 v41, 0x3fb8aa3b, v41
	v_sub_f32_e32 v42, v109, v93
	v_cvt_pk_bf16_f32 v39, v43, v44
	v_exp_f32_e32 v41, v41
	v_mul_f32_e32 v42, 0x3fb8aa3b, v42
	v_sub_f32_e32 v43, v106, v93
	v_exp_f32_e32 v42, v42
	v_mul_f32_e32 v43, 0x3fb8aa3b, v43
	v_add_f32_e32 v44, v40, v45
	v_sub_f32_e32 v45, v102, v93
	v_sub_f32_e32 v46, v103, v93
	v_exp_f32_e32 v43, v43
	v_mul_f32_e32 v45, 0x3fb8aa3b, v45
	v_mul_f32_e32 v46, 0x3fb8aa3b, v46
	v_exp_f32_e32 v45, v45
	v_exp_f32_e32 v46, v46
	v_sub_f32_e32 v47, v104, v93
	v_sub_f32_e32 v51, v105, v93
	v_add_f32_e32 v44, v41, v44
	v_mul_f32_e32 v47, 0x3fb8aa3b, v47
	v_mul_f32_e32 v51, 0x3fb8aa3b, v51
	v_add_f32_e32 v44, v42, v44
	v_exp_f32_e32 v47, v47
	v_exp_f32_e32 v51, v51
	v_add_f32_e32 v44, v43, v44
	v_add_f32_e32 v44, v45, v44
	v_cvt_pk_bf16_f32 v40, v40, v41
	v_cvt_pk_bf16_f32 v41, v42, v43
	v_cvt_pk_bf16_f32 v42, v45, v46
	v_sub_f32_e32 v45, v115, v93
	v_add_f32_e32 v44, v46, v44
	v_mul_f32_e32 v45, 0x3fb8aa3b, v45
	v_sub_f32_e32 v46, v116, v93
	v_add_f32_e32 v44, v47, v44
	v_cvt_pk_bf16_f32 v43, v47, v51
	v_exp_f32_e32 v45, v45
	v_mul_f32_e32 v46, 0x3fb8aa3b, v46
	v_sub_f32_e32 v47, v117, v93
	v_add_f32_e32 v44, v51, v44
	v_exp_f32_e32 v46, v46
	v_mul_f32_e32 v47, 0x3fb8aa3b, v47
	v_sub_f32_e32 v51, v114, v93
	v_exp_f32_e32 v47, v47
	v_mul_f32_e32 v51, 0x3fb8aa3b, v51
	v_sub_f32_e32 v52, v110, v93
	v_exp_f32_e32 v51, v51
	v_mul_f32_e32 v52, 0x3fb8aa3b, v52
	v_sub_f32_e32 v53, v111, v93
	v_add_f32_e32 v44, v45, v44
	v_exp_f32_e32 v52, v52
	v_mul_f32_e32 v53, 0x3fb8aa3b, v53
	v_sub_f32_e32 v54, v112, v93
	v_add_f32_e32 v44, v46, v44
	v_exp_f32_e32 v53, v53
	v_mul_f32_e32 v54, 0x3fb8aa3b, v54
	v_sub_f32_e32 v55, v113, v93
	v_add_f32_e32 v44, v47, v44
	v_exp_f32_e32 v54, v54
	v_mul_f32_e32 v55, 0x3fb8aa3b, v55
	v_add_f32_e32 v44, v51, v44
	v_exp_f32_e32 v55, v55
	v_add_f32_e32 v44, v52, v44
	v_add_f32_e32 v44, v53, v44
	v_add_f32_e32 v44, v54, v44
	v_add_f32_e32 v66, v55, v44
	v_cvt_pk_bf16_f32 v44, v45, v46
	v_cvt_pk_bf16_f32 v45, v47, v51
	v_sub_f32_e32 v51, v123, v93
	v_mul_f32_e32 v51, 0x3fb8aa3b, v51
	v_exp_f32_e32 v51, v51
	v_cvt_pk_bf16_f32 v46, v52, v53
	v_sub_f32_e32 v52, v124, v93
	v_mul_f32_e32 v52, 0x3fb8aa3b, v52
	v_sub_f32_e32 v53, v125, v93
	v_cvt_pk_bf16_f32 v47, v54, v55
	v_exp_f32_e32 v52, v52
	v_mul_f32_e32 v53, 0x3fb8aa3b, v53
	v_sub_f32_e32 v54, v122, v93
	v_exp_f32_e32 v53, v53
	v_mul_f32_e32 v54, 0x3fb8aa3b, v54
	v_add_f32_e32 v55, v51, v66
	v_sub_f32_e32 v66, v118, v93
	v_exp_f32_e32 v54, v54
	v_mul_f32_e32 v66, 0x3fb8aa3b, v66
	v_sub_f32_e32 v67, v119, v93
	v_exp_f32_e32 v66, v66
	v_mul_f32_e32 v67, 0x3fb8aa3b, v67
	v_sub_f32_e32 v68, v120, v93
	v_add_f32_e32 v55, v52, v55
	v_exp_f32_e32 v67, v67
	v_mul_f32_e32 v68, 0x3fb8aa3b, v68
	v_sub_f32_e32 v69, v121, v93
	v_add_f32_e32 v55, v53, v55
	v_exp_f32_e32 v68, v68
	v_mul_f32_e32 v69, 0x3fb8aa3b, v69
	v_sub_f32_e32 v49, v49, v93
	v_add_f32_e32 v55, v54, v55
	v_exp_f32_e32 v69, v69
	v_mul_f32_e32 v49, 0x3fb8aa3b, v49
	v_sub_f32_e32 v50, v50, v93
	v_add_f32_e32 v55, v66, v55
	v_exp_f32_e32 v49, v49
	v_mul_f32_e32 v50, 0x3fb8aa3b, v50
	v_sub_f32_e32 v70, v86, v93
	v_add_f32_e32 v55, v67, v55
	v_exp_f32_e32 v50, v50
	v_mul_f32_e32 v70, 0x3fb8aa3b, v70
	v_sub_f32_e32 v71, v87, v93
	v_add_f32_e32 v55, v68, v55
	v_exp_f32_e32 v70, v70
	v_mul_f32_e32 v71, 0x3fb8aa3b, v71
	v_sub_f32_e32 v72, v88, v93
	v_add_f32_e32 v55, v69, v55
	v_exp_f32_e32 v71, v71
	v_mul_f32_e32 v72, 0x3fb8aa3b, v72
	v_sub_f32_e32 v73, v89, v93
	v_add_f32_e32 v55, v49, v55
	v_exp_f32_e32 v72, v72
	v_mul_f32_e32 v73, 0x3fb8aa3b, v73
	v_sub_f32_e32 v74, v90, v93
	v_add_f32_e32 v55, v50, v55
	v_exp_f32_e32 v73, v73
	v_mul_f32_e32 v74, 0x3fb8aa3b, v74
	v_sub_f32_e32 v48, v48, v93
	v_add_f32_e32 v55, v70, v55
	v_exp_f32_e32 v74, v74
	v_mul_f32_e32 v48, 0x3fb8aa3b, v48
	v_add_f32_e32 v55, v71, v55
	v_exp_f32_e32 v75, v48
	v_add_f32_e32 v48, v72, v55
	v_add_f32_e32 v48, v73, v48
	v_add_f32_e32 v48, v74, v48
	v_add_f32_e32 v48, v75, v48
	ds_bpermute_b32 v76, v195, v48
	v_cvt_pk_bf16_f32 v53, v53, v54
	v_cvt_pk_bf16_f32 v54, v66, v67
	v_bfe_u32 v87, v61, 1, 1
	v_and_b32_e32 v61, 8, v92
	s_waitcnt lgkmcnt(0)
	v_add_f32_e32 v66, v48, v76
	ds_bpermute_b32 v67, v196, v66
	v_cvt_pk_bf16_f32 v55, v68, v69
	v_cvt_pk_bf16_f32 v48, v49, v50
	v_cvt_pk_bf16_f32 v49, v70, v71
	v_cvt_pk_bf16_f32 v50, v72, v73
	s_waitcnt lgkmcnt(0)
	v_add_f32_e32 v82, v66, v67
	v_lshlrev_b32_e32 v66, 2, v91
	v_and_b32_e32 v86, 4, v66
	v_or_b32_e32 v66, v58, v65
	v_lshl_or_b32 v88, v66, 7, v61
	v_bitop3_b32 v61, v86, v87, v65 bitop3:0x36
	v_div_scale_f32 v78, s[10:11], v82, v82, 1.0
	v_lshl_or_b32 v61, v61, 4, v88
	v_rcp_f32_e32 v79, v78
	v_add_u32_e32 v68, s5, v61
	ds_read_b64_tr_b16 v[66:67], v68
	ds_read_b64_tr_b16 v[68:69], v68 offset:2048
	v_add_u32_e32 v72, s9, v61
	v_fma_f32 v70, -v78, v79, 1.0
	v_fmac_f32_e32 v79, v70, v79
	ds_read_b64_tr_b16 v[70:71], v72
	ds_read_b64_tr_b16 v[72:73], v72 offset:2048
	s_waitcnt lgkmcnt(2)
; #define LAS __attribute__((address_space(3)))
; __device__ __forceinline__ float clamp8(float v) { return __builtin_amdgcn_fmed3f(v, -440.f, 440.f); }
; __device__ __forceinline__ void unit(const bf16_t* __restrict__ proj, const float* __restrict__ rpb, bf16_t* __restrict__ ymix, LAS unsigned char* lds, int u, const int tid_in) {
;     ...
;         const unsigned sl = (((unsigned)g & 1u) << 2) | qp;
;         unsigned char* op = (unsigned char*)ymix + (size_t)tq * D + head * 64 + 4 * g;
; #pragma unroll
;         for (int db = 0; db < 4; ++db) {
;             const unsigned vb = 128u * (4u * (unsigned)g + qp) + 16u * ((2u * db + (p >> 1)) ^ sl) + 8u * (p & 1u);
;             f32x4 y = (f32x4){0.f, 0.f, 0.f, 0.f};
; #pragma unroll
;             for (int kk = 0; kk < 8; ++kk) {
;                 const unsigned so = (unsigned)((rs + kk) % 9) * 8192u + 128u * (unsigned)cb;
;                 const ret::s16x4 lo = __builtin_amdgcn_ds_read_tr16_b64_v4i16((LAS ret::s16x4*)(lds + LVR + so + vb));
;                 const ret::s16x4 hi = __builtin_amdgcn_ds_read_tr16_b64_v4i16((LAS ret::s16x4*)(lds + LVR + so + 2048u + vb));
;                 y = __builtin_amdgcn_mfma_f32_16x16x32_bf16(__builtin_shufflevector(lo, hi, 0, 1, 2, 3, 4, 5, 6, 7), pt[kk], y, 0, 0, 0);
;             }
;             const float inv16 = inv * S_H8;
;             int o = __builtin_amdgcn_cvt_pk_fp8_f32(clamp8(y[0] * inv16), clamp8(y[1] * inv16), 0, false); o = __builtin_amdgcn_cvt_pk_fp8_f32(clamp8(y[2] * inv16), clamp8(y[3] * inv16), o, true);
;             *(unsigned*)(op + 16 * db) = (unsigned)o;
;         }
	v_mfma_f32_16x16x32_bf16 v[66:69], v[66:69], v[24:27], 0
	s_add_i32 s10, s50, s22
	v_add_u32_e32 v76, s10, v61
	v_cvt_pk_bf16_f32 v52, v51, v52
	v_cvt_pk_bf16_f32 v51, v74, v75
	ds_read_b64_tr_b16 v[74:75], v76
	ds_read_b64_tr_b16 v[76:77], v76 offset:2048
	s_waitcnt lgkmcnt(2)
	v_mfma_f32_16x16x32_bf16 v[66:69], v[70:73], v[28:31], v[66:69]
	s_add_i32 s11, s50, s23
	v_add_u32_e32 v72, s11, v61
	ds_read_b64_tr_b16 v[70:71], v72
	ds_read_b64_tr_b16 v[72:73], v72 offset:2048
	s_waitcnt lgkmcnt(2)
	v_mfma_f32_16x16x32_bf16 v[66:69], v[74:77], v[32:35], v[66:69]
	v_add_u32_e32 v76, s12, v61
	ds_read_b64_tr_b16 v[74:75], v76
	ds_read_b64_tr_b16 v[76:77], v76 offset:2048
	v_div_scale_f32 v80, vcc, 1.0, v82, 1.0
	s_waitcnt lgkmcnt(2)
	v_mfma_f32_16x16x32_bf16 v[66:69], v[70:73], v[36:39], v[66:69]
	v_mul_f32_e32 v81, v80, v79
	v_add_u32_e32 v72, s13, v61
	v_fma_f32 v83, -v78, v81, v80
	ds_read_b64_tr_b16 v[70:71], v72
	ds_read_b64_tr_b16 v[72:73], v72 offset:2048
	v_fmac_f32_e32 v81, v83, v79
	s_waitcnt lgkmcnt(2)
	v_mfma_f32_16x16x32_bf16 v[66:69], v[74:77], v[40:43], v[66:69]
	s_add_i32 s15, s50, s57
	v_fma_f32 v78, -v78, v81, v80
	v_add_u32_e32 v76, s14, v61
	v_add_u32_e32 v61, s15, v61
	v_div_fmas_f32 v83, v78, v79, v81
	ds_read_b64_tr_b16 v[74:75], v76
	ds_read_b64_tr_b16 v[76:77], v76 offset:2048
	ds_read_b64_tr_b16 v[78:79], v61
	ds_read_b64_tr_b16 v[80:81], v61 offset:2048
	v_ashrrev_i32_e32 v61, 31, v60
	v_lshlrev_b64 v[60:61], 10, v[60:61]
	s_waitcnt lgkmcnt(4)
	v_mfma_f32_16x16x32_bf16 v[66:69], v[70:73], v[44:47], v[66:69]
	v_div_fixup_f32 v70, v83, v82, 1.0
	v_lshl_add_u64 v[60:61], s[36:37], 0, v[60:61]
	v_lshl_add_u64 v[60:61], v[60:61], 0, v[58:59]
	v_mul_f32_e32 v58, 0x41800000, v70
	v_or_b32_e32 v70, 2, v87
	v_bitop3_b32 v70, v86, v70, v65 bitop3:0x36
	v_lshl_or_b32 v89, v70, 4, v88
	v_add_u32_e32 v72, s5, v89
	ds_read_b64_tr_b16 v[70:71], v72
	ds_read_b64_tr_b16 v[72:73], v72 offset:2048
	s_waitcnt lgkmcnt(4)
	v_mfma_f32_16x16x32_bf16 v[66:69], v[74:77], v[52:55], v[66:69]
	v_add_u32_e32 v76, s9, v89
	ds_read_b64_tr_b16 v[74:75], v76
	ds_read_b64_tr_b16 v[76:77], v76 offset:2048
	v_add_u32_e32 v84, s11, v89
	s_waitcnt lgkmcnt(2)
	v_mfma_f32_16x16x32_bf16 v[70:73], v[70:73], v[24:27], 0
	v_mov_b32_e32 v90, v59
	v_mov_b32_e32 v91, v59
	s_add_i32 s8, s54, -7
	v_mfma_f32_16x16x32_bf16 v[66:69], v[78:81], v[48:51], v[66:69]
	v_add_u32_e32 v80, s10, v89
	ds_read_b64_tr_b16 v[78:79], v80
	ds_read_b64_tr_b16 v[80:81], v80 offset:2048
	ds_read_b64_tr_b16 v[82:83], v84
	ds_read_b64_tr_b16 v[84:85], v84 offset:2048
	s_waitcnt lgkmcnt(4)
	v_mfma_f32_16x16x32_bf16 v[70:73], v[74:77], v[28:31], v[70:73]
	v_add_u32_e32 v76, s12, v89
	ds_read_b64_tr_b16 v[74:75], v76
	ds_read_b64_tr_b16 v[76:77], v76 offset:2048
	v_mul_f32_e32 v66, v66, v58
	s_waitcnt lgkmcnt(4)
	v_mfma_f32_16x16x32_bf16 v[70:73], v[78:81], v[32:35], v[70:73]
	v_add_u32_e32 v80, s13, v89
	ds_read_b64_tr_b16 v[78:79], v80
	ds_read_b64_tr_b16 v[80:81], v80 offset:2048
	v_mul_f32_e32 v67, v67, v58
	s_waitcnt lgkmcnt(4)
	v_mfma_f32_16x16x32_bf16 v[70:73], v[82:85], v[36:39], v[70:73]
	v_add_u32_e32 v84, s14, v89
	ds_read_b64_tr_b16 v[82:83], v84
	ds_read_b64_tr_b16 v[84:85], v84 offset:2048
	v_med3_f32 v66, v66, s41, v63
	s_waitcnt lgkmcnt(4)
	v_mfma_f32_16x16x32_bf16 v[70:73], v[74:77], v[40:43], v[70:73]
	v_add_u32_e32 v76, s15, v89
	v_med3_f32 v67, v67, s41, v63
	ds_read_b64_tr_b16 v[74:75], v76
	ds_read_b64_tr_b16 v[76:77], v76 offset:2048
	s_waitcnt lgkmcnt(4)
	v_mfma_f32_16x16x32_bf16 v[70:73], v[78:81], v[44:47], v[70:73]
	v_cvt_pk_fp8_f32 v90, v66, v67
	v_mul_f32_e32 v66, v68, v58
	v_mul_f32_e32 v67, v69, v58
	s_waitcnt lgkmcnt(2)
	v_mfma_f32_16x16x32_bf16 v[70:73], v[82:85], v[52:55], v[70:73]
	v_med3_f32 v66, v66, s41, v63
	v_med3_f32 v67, v67, s41, v63
	v_cvt_pk_fp8_f32 v90, v66, v67 op_sel:[0,0,1]
	s_waitcnt lgkmcnt(0)
	v_mfma_f32_16x16x32_bf16 v[66:69], v[74:77], v[48:51], v[70:73]
	s_add_i32 s52, s52, 1
	s_add_i32 s51, s51, 2
	s_cmp_lg_u32 s52, 16
	v_or_b32_e32 v70, 4, v87
	v_bitop3_b32 v70, v86, v70, v65 bitop3:0x36
	v_lshl_or_b32 v89, v70, 4, v88
	v_add_u32_e32 v72, s5, v89
	ds_read_b64_tr_b16 v[70:71], v72
	ds_read_b64_tr_b16 v[72:73], v72 offset:2048
	v_add_u32_e32 v76, s9, v89
	ds_read_b64_tr_b16 v[74:75], v76
	ds_read_b64_tr_b16 v[76:77], v76 offset:2048
	s_waitcnt lgkmcnt(2)
; #define LAS __attribute__((address_space(3)))
; __device__ __forceinline__ float clamp8(float v) { return __builtin_amdgcn_fmed3f(v, -440.f, 440.f); }
; __device__ __forceinline__ void unit(const bf16_t* __restrict__ proj, const float* __restrict__ rpb, bf16_t* __restrict__ ymix, LAS unsigned char* lds, int u, const int tid_in) {
;     ...
; #pragma unroll
;         for (int db = 0; db < 4; ++db) {
;             const unsigned vb = 128u * (4u * (unsigned)g + qp) + 16u * ((2u * db + (p >> 1)) ^ sl) + 8u * (p & 1u);
;             f32x4 y = (f32x4){0.f, 0.f, 0.f, 0.f};
; #pragma unroll
;             for (int kk = 0; kk < 8; ++kk) {
;                 const unsigned so = (unsigned)((rs + kk) % 9) * 8192u + 128u * (unsigned)cb;
;                 const ret::s16x4 lo = __builtin_amdgcn_ds_read_tr16_b64_v4i16((LAS ret::s16x4*)(lds + LVR + so + vb));
;                 const ret::s16x4 hi = __builtin_amdgcn_ds_read_tr16_b64_v4i16((LAS ret::s16x4*)(lds + LVR + so + 2048u + vb));
;                 y = __builtin_amdgcn_mfma_f32_16x16x32_bf16(__builtin_shufflevector(lo, hi, 0, 1, 2, 3, 4, 5, 6, 7), pt[kk], y, 0, 0, 0);
;             }
;             const float inv16 = inv * S_H8;
;             int o = __builtin_amdgcn_cvt_pk_fp8_f32(clamp8(y[0] * inv16), clamp8(y[1] * inv16), 0, false); o = __builtin_amdgcn_cvt_pk_fp8_f32(clamp8(y[2] * inv16), clamp8(y[3] * inv16), o, true);
;             *(unsigned*)(op + 16 * db) = (unsigned)o;
;         }
	v_mfma_f32_16x16x32_bf16 v[70:73], v[70:73], v[24:27], 0
	v_add_u32_e32 v80, s10, v89
	ds_read_b64_tr_b16 v[78:79], v80
	ds_read_b64_tr_b16 v[80:81], v80 offset:2048
	v_add_u32_e32 v84, s11, v89
	s_waitcnt lgkmcnt(2)
	v_mfma_f32_16x16x32_bf16 v[70:73], v[74:77], v[28:31], v[70:73]
	ds_read_b64_tr_b16 v[82:83], v84
	ds_read_b64_tr_b16 v[84:85], v84 offset:2048
	v_add_u32_e32 v76, s12, v89
	ds_read_b64_tr_b16 v[74:75], v76
	ds_read_b64_tr_b16 v[76:77], v76 offset:2048
	s_waitcnt lgkmcnt(4)
	v_mfma_f32_16x16x32_bf16 v[70:73], v[78:81], v[32:35], v[70:73]
	v_add_u32_e32 v80, s13, v89
	ds_read_b64_tr_b16 v[78:79], v80
	ds_read_b64_tr_b16 v[80:81], v80 offset:2048
	v_mul_f32_e32 v66, v66, v58
	s_waitcnt lgkmcnt(4)
	v_mfma_f32_16x16x32_bf16 v[70:73], v[82:85], v[36:39], v[70:73]
	v_add_u32_e32 v84, s14, v89
	ds_read_b64_tr_b16 v[82:83], v84
	ds_read_b64_tr_b16 v[84:85], v84 offset:2048
	v_mul_f32_e32 v67, v67, v58
	s_waitcnt lgkmcnt(4)
	v_mfma_f32_16x16x32_bf16 v[70:73], v[74:77], v[40:43], v[70:73]
	v_add_u32_e32 v76, s15, v89
	v_med3_f32 v66, v66, s41, v63
	v_med3_f32 v67, v67, s41, v63
	s_waitcnt lgkmcnt(2)
	v_mfma_f32_16x16x32_bf16 v[70:73], v[78:81], v[44:47], v[70:73]
	ds_read_b64_tr_b16 v[74:75], v76
	ds_read_b64_tr_b16 v[76:77], v76 offset:2048
	v_cvt_pk_fp8_f32 v91, v66, v67
	v_mul_f32_e32 v66, v68, v58
	s_waitcnt lgkmcnt(2)
	v_mfma_f32_16x16x32_bf16 v[70:73], v[82:85], v[52:55], v[70:73]
	v_mul_f32_e32 v67, v69, v58
	v_med3_f32 v66, v66, s41, v63
	v_med3_f32 v67, v67, s41, v63
	v_cvt_pk_fp8_f32 v91, v66, v67 op_sel:[0,0,1]
	s_waitcnt lgkmcnt(0)
	v_mfma_f32_16x16x32_bf16 v[66:69], v[74:77], v[48:51], v[70:73]
	v_mov_b32_e32 v82, v59
	s_nop 1
	v_or_b32_e32 v70, 6, v87
	v_bitop3_b32 v65, v86, v70, v65 bitop3:0x36
	v_lshl_or_b32 v65, v65, 4, v88
	v_add_u32_e32 v72, s5, v65
	ds_read_b64_tr_b16 v[70:71], v72
	ds_read_b64_tr_b16 v[72:73], v72 offset:2048
	v_add_u32_e32 v76, s9, v65
	ds_read_b64_tr_b16 v[74:75], v76
	ds_read_b64_tr_b16 v[76:77], v76 offset:2048
	s_waitcnt lgkmcnt(2)
	v_mfma_f32_16x16x32_bf16 v[24:27], v[70:73], v[24:27], 0
	v_add_u32_e32 v80, s10, v65
	ds_read_b64_tr_b16 v[78:79], v80
	ds_read_b64_tr_b16 v[80:81], v80 offset:2048
	v_add_u32_e32 v72, s11, v65
	s_waitcnt lgkmcnt(2)
	v_mfma_f32_16x16x32_bf16 v[24:27], v[74:77], v[28:31], v[24:27]
	ds_read_b64_tr_b16 v[70:71], v72
	ds_read_b64_tr_b16 v[72:73], v72 offset:2048
	v_add_u32_e32 v30, s12, v65
	ds_read_b64_tr_b16 v[28:29], v30
	ds_read_b64_tr_b16 v[30:31], v30 offset:2048
	s_waitcnt lgkmcnt(4)
	v_mfma_f32_16x16x32_bf16 v[24:27], v[78:81], v[32:35], v[24:27]
	v_add_u32_e32 v34, s13, v65
	ds_read_b64_tr_b16 v[32:33], v34
	ds_read_b64_tr_b16 v[34:35], v34 offset:2048
	v_mul_f32_e32 v66, v58, v66
	s_waitcnt lgkmcnt(4)
	v_mfma_f32_16x16x32_bf16 v[24:27], v[70:73], v[36:39], v[24:27]
	v_add_u32_e32 v38, s14, v65
	ds_read_b64_tr_b16 v[36:37], v38
	ds_read_b64_tr_b16 v[38:39], v38 offset:2048
	v_mul_f32_e32 v67, v58, v67
	s_waitcnt lgkmcnt(4)
	v_mfma_f32_16x16x32_bf16 v[24:27], v[28:31], v[40:43], v[24:27]
	v_add_u32_e32 v30, s15, v65
	ds_read_b64_tr_b16 v[28:29], v30
	ds_read_b64_tr_b16 v[30:31], v30 offset:2048
	v_med3_f32 v66, v66, s41, v63
	s_waitcnt lgkmcnt(4)
	v_mfma_f32_16x16x32_bf16 v[24:27], v[32:35], v[44:47], v[24:27]
	v_med3_f32 v67, v67, s41, v63
	v_cvt_pk_fp8_f32 v82, v66, v67
	v_mul_f32_e32 v32, v58, v68
	s_waitcnt lgkmcnt(2)
	v_mfma_f32_16x16x32_bf16 v[24:27], v[36:39], v[52:55], v[24:27]
	v_mul_f32_e32 v33, v58, v69
	v_med3_f32 v32, v32, s41, v63
	v_med3_f32 v33, v33, s41, v63
	s_waitcnt lgkmcnt(0)
	v_mfma_f32_16x16x32_bf16 v[24:27], v[28:31], v[48:51], v[24:27]
	v_mov_b32_e32 v28, v59
	v_cvt_pk_fp8_f32 v82, v32, v33 op_sel:[0,0,1]
	s_nop 5
	v_mul_f32_e32 v24, v58, v24
	v_mul_f32_e32 v25, v58, v25
	v_med3_f32 v24, v24, s41, v63
	v_med3_f32 v25, v25, s41, v63
	v_cvt_pk_fp8_f32 v28, v24, v25
	v_mul_f32_e32 v24, v58, v26
	v_mul_f32_e32 v25, v58, v27
	v_med3_f32 v24, v24, s41, v63
	v_med3_f32 v25, v25, s41, v63
	v_cvt_pk_fp8_f32 v28, v24, v25 op_sel:[0,0,1]
	global_store_dword v[60:61], v90, off
	global_store_dword v[60:61], v91, off offset:16
	global_store_dword v[60:61], v82, off offset:32
	global_store_dword v[60:61], v28, off offset:48
	s_waitcnt vmcnt(4)
	v_mov_b64_e32 v[26:27], v[22:23]
	v_mov_b64_e32 v[30:31], v[18:19]
	v_mov_b64_e32 v[24:25], v[20:21]
	v_mov_b64_e32 v[28:29], v[16:17]
	s_cbranch_scc0 .LBB0_313
